# v10
# baseline (speedup 1.0000x reference)
.LBB0_40:
	s_lshl_b32 s12, s30, 2
	s_add_u32 s8, s16, s12
	s_addc_u32 s9, s17, 0
	s_waitcnt vmcnt(13)
	v_lshlrev_b32_e32 v42, 4, v209
	s_add_u32 s12, s18, s12
	s_addc_u32 s13, s19, 0
	global_load_dwordx4 v[38:41], v42, s[8:9]
	global_load_dwordx4 v[34:37], v42, s[12:13]
	s_lshl_b32 s36, s27, 3
	s_add_i32 s36, s36, s31
	s_mul_i32 s37, s36, 0x210
	s_add_i32 s37, s37, 0x23440
	s_mov_b32 s14, 0xaaaaaaaa
	s_mov_b32 s15, 0xaaaaaaaa
	s_mov_b32 s24, 0xcccccccc
	s_mov_b32 s25, 0xcccccccc
	v_mov_b32_e32 v42, v218
	s_nop 1
	v_max_f32_dpp v42, v42, v42 quad_perm:[1,0,3,2] row_mask:0xf bank_mask:0xf
	s_nop 1
	v_max_f32_dpp v42, v42, v42 quad_perm:[2,3,0,1] row_mask:0xf bank_mask:0xf
	s_nop 1
	v_max_f32_dpp v42, v42, v42 row_half_mirror row_mask:0xf bank_mask:0xf
	s_nop 1
	v_max_f32_dpp v42, v42, v42 row_mirror row_mask:0xf bank_mask:0xf
	v_sub_f32_e32 v44, v218, v42
	v_exp_f32_e32 v44, v44
	v_and_b32_e32 v47, 3, v131
	v_lshl_add_u32 v47, v47, 2, v203
	v_mul_f32_e32 v43, v219, v44
	v_pk_mul_f32 v[48:49], v[198:199], v[44:45] op_sel_hi:[1,0]
	v_pk_mul_f32 v[50:51], v[196:197], v[44:45] op_sel_hi:[1,0]
	v_pk_mul_f32 v[52:53], v[194:195], v[44:45] op_sel_hi:[1,0]
	v_pk_mul_f32 v[54:55], v[192:193], v[44:45] op_sel_hi:[1,0]
	v_pk_mul_f32 v[56:57], v[190:191], v[44:45] op_sel_hi:[1,0]
	v_pk_mul_f32 v[58:59], v[188:189], v[44:45] op_sel_hi:[1,0]
	v_pk_mul_f32 v[60:61], v[186:187], v[44:45] op_sel_hi:[1,0]
	v_pk_mul_f32 v[62:63], v[184:185], v[44:45] op_sel_hi:[1,0]
	v_pk_mul_f32 v[64:65], v[182:183], v[44:45] op_sel_hi:[1,0]
	v_pk_mul_f32 v[66:67], v[180:181], v[44:45] op_sel_hi:[1,0]
	v_pk_mul_f32 v[68:69], v[178:179], v[44:45] op_sel_hi:[1,0]
	v_pk_mul_f32 v[70:71], v[168:169], v[44:45] op_sel_hi:[1,0]
	v_pk_mul_f32 v[72:73], v[150:151], v[44:45] op_sel_hi:[1,0]
	v_pk_mul_f32 v[74:75], v[140:141], v[44:45] op_sel_hi:[1,0]
	v_pk_mul_f32 v[76:77], v[138:139], v[44:45] op_sel_hi:[1,0]
	v_pk_mul_f32 v[78:79], v[136:137], v[44:45] op_sel_hi:[1,0]
	v_add_u32_e32 v47, s37, v47
	v_add_f32_dpp v43, v43, v43 row_shr:1 row_mask:0xf bank_mask:0xf
	v_cndmask_b32_e64 v80, v48, v49, s[14:15]
	v_cndmask_b32_e64 v49, v49, v48, s[14:15]
	v_cndmask_b32_e64 v81, v50, v51, s[14:15]
	v_cndmask_b32_e64 v51, v51, v50, s[14:15]
	v_cndmask_b32_e64 v82, v52, v53, s[14:15]
	v_cndmask_b32_e64 v53, v53, v52, s[14:15]
	v_cndmask_b32_e64 v83, v54, v55, s[14:15]
	v_cndmask_b32_e64 v55, v55, v54, s[14:15]
	v_cndmask_b32_e64 v84, v56, v57, s[14:15]
	v_cndmask_b32_e64 v57, v57, v56, s[14:15]
	v_cndmask_b32_e64 v85, v58, v59, s[14:15]
	v_cndmask_b32_e64 v59, v59, v58, s[14:15]
	v_cndmask_b32_e64 v86, v60, v61, s[14:15]
	v_cndmask_b32_e64 v61, v61, v60, s[14:15]
	v_cndmask_b32_e64 v87, v62, v63, s[14:15]
	v_cndmask_b32_e64 v63, v63, v62, s[14:15]
	v_cndmask_b32_e64 v88, v64, v65, s[14:15]
	v_cndmask_b32_e64 v65, v65, v64, s[14:15]
	v_cndmask_b32_e64 v89, v66, v67, s[14:15]
	v_cndmask_b32_e64 v67, v67, v66, s[14:15]
	v_cndmask_b32_e64 v90, v68, v69, s[14:15]
	v_cndmask_b32_e64 v69, v69, v68, s[14:15]
	v_cndmask_b32_e64 v91, v70, v71, s[14:15]
	v_cndmask_b32_e64 v71, v71, v70, s[14:15]
	v_cndmask_b32_e64 v92, v72, v73, s[14:15]
	v_cndmask_b32_e64 v73, v73, v72, s[14:15]
	v_cndmask_b32_e64 v93, v74, v75, s[14:15]
	v_cndmask_b32_e64 v75, v75, v74, s[14:15]
	v_cndmask_b32_e64 v94, v76, v77, s[14:15]
	v_cndmask_b32_e64 v77, v77, v76, s[14:15]
	v_cndmask_b32_e64 v95, v78, v79, s[14:15]
	v_cndmask_b32_e64 v79, v79, v78, s[14:15]
	v_add_f32_dpp v43, v43, v43 row_shr:2 row_mask:0xf bank_mask:0xf
	v_add_f32_dpp v48, v49, v80 quad_perm:[1,0,3,2] row_mask:0xf bank_mask:0xf
	v_add_f32_dpp v50, v51, v81 quad_perm:[1,0,3,2] row_mask:0xf bank_mask:0xf
	v_add_f32_dpp v52, v53, v82 quad_perm:[1,0,3,2] row_mask:0xf bank_mask:0xf
	v_add_f32_dpp v54, v55, v83 quad_perm:[1,0,3,2] row_mask:0xf bank_mask:0xf
	v_add_f32_dpp v56, v57, v84 quad_perm:[1,0,3,2] row_mask:0xf bank_mask:0xf
	v_add_f32_dpp v58, v59, v85 quad_perm:[1,0,3,2] row_mask:0xf bank_mask:0xf
	v_add_f32_dpp v60, v61, v86 quad_perm:[1,0,3,2] row_mask:0xf bank_mask:0xf
	v_add_f32_dpp v62, v63, v87 quad_perm:[1,0,3,2] row_mask:0xf bank_mask:0xf
	v_add_f32_dpp v64, v65, v88 quad_perm:[1,0,3,2] row_mask:0xf bank_mask:0xf
	v_add_f32_dpp v66, v67, v89 quad_perm:[1,0,3,2] row_mask:0xf bank_mask:0xf
	v_add_f32_dpp v68, v69, v90 quad_perm:[1,0,3,2] row_mask:0xf bank_mask:0xf
	v_add_f32_dpp v70, v71, v91 quad_perm:[1,0,3,2] row_mask:0xf bank_mask:0xf
	v_add_f32_dpp v72, v73, v92 quad_perm:[1,0,3,2] row_mask:0xf bank_mask:0xf
	v_add_f32_dpp v74, v75, v93 quad_perm:[1,0,3,2] row_mask:0xf bank_mask:0xf
	v_add_f32_dpp v76, v77, v94 quad_perm:[1,0,3,2] row_mask:0xf bank_mask:0xf
	v_add_f32_dpp v78, v79, v95 quad_perm:[1,0,3,2] row_mask:0xf bank_mask:0xf
	v_add_f32_dpp v43, v43, v43 row_shr:4 row_mask:0xf bank_mask:0xf
	v_cndmask_b32_e64 v80, v48, v50, s[24:25]
	v_cndmask_b32_e64 v50, v50, v48, s[24:25]
	v_cndmask_b32_e64 v81, v52, v54, s[24:25]
	v_cndmask_b32_e64 v54, v54, v52, s[24:25]
	v_cndmask_b32_e64 v82, v56, v58, s[24:25]
	v_cndmask_b32_e64 v58, v58, v56, s[24:25]
	v_cndmask_b32_e64 v83, v60, v62, s[24:25]
	v_cndmask_b32_e64 v62, v62, v60, s[24:25]
	v_cndmask_b32_e64 v84, v64, v66, s[24:25]
	v_cndmask_b32_e64 v66, v66, v64, s[24:25]
	v_cndmask_b32_e64 v85, v68, v70, s[24:25]
	v_cndmask_b32_e64 v70, v70, v68, s[24:25]
	v_cndmask_b32_e64 v86, v72, v74, s[24:25]
	v_cndmask_b32_e64 v74, v74, v72, s[24:25]
	v_cndmask_b32_e64 v87, v76, v78, s[24:25]
	v_cndmask_b32_e64 v78, v78, v76, s[24:25]
	v_add_f32_dpp v43, v43, v43 row_shr:8 row_mask:0xf bank_mask:0xf
	v_add_f32_dpp v48, v50, v80 quad_perm:[2,3,0,1] row_mask:0xf bank_mask:0xf
	v_add_f32_dpp v52, v54, v81 quad_perm:[2,3,0,1] row_mask:0xf bank_mask:0xf
	v_add_f32_dpp v56, v58, v82 quad_perm:[2,3,0,1] row_mask:0xf bank_mask:0xf
	v_add_f32_dpp v60, v62, v83 quad_perm:[2,3,0,1] row_mask:0xf bank_mask:0xf
	v_add_f32_dpp v64, v66, v84 quad_perm:[2,3,0,1] row_mask:0xf bank_mask:0xf
	v_add_f32_dpp v68, v70, v85 quad_perm:[2,3,0,1] row_mask:0xf bank_mask:0xf
	v_add_f32_dpp v72, v74, v86 quad_perm:[2,3,0,1] row_mask:0xf bank_mask:0xf
	v_add_f32_dpp v76, v78, v87 quad_perm:[2,3,0,1] row_mask:0xf bank_mask:0xf
	v_add_f32_dpp v48, v48, v48 row_shr:4 row_mask:0xf bank_mask:0xf
	v_add_f32_dpp v52, v52, v52 row_shr:4 row_mask:0xf bank_mask:0xf
	v_add_f32_dpp v56, v56, v56 row_shr:4 row_mask:0xf bank_mask:0xf
	v_add_f32_dpp v60, v60, v60 row_shr:4 row_mask:0xf bank_mask:0xf
	v_add_f32_dpp v64, v64, v64 row_shr:4 row_mask:0xf bank_mask:0xf
	v_add_f32_dpp v68, v68, v68 row_shr:4 row_mask:0xf bank_mask:0xf
	v_add_f32_dpp v72, v72, v72 row_shr:4 row_mask:0xf bank_mask:0xf
	v_add_f32_dpp v76, v76, v76 row_shr:4 row_mask:0xf bank_mask:0xf
	v_add_f32_dpp v48, v48, v48 row_shr:8 row_mask:0xf bank_mask:0xf
	v_add_f32_dpp v52, v52, v52 row_shr:8 row_mask:0xf bank_mask:0xf
	v_add_f32_dpp v56, v56, v56 row_shr:8 row_mask:0xf bank_mask:0xf
	v_add_f32_dpp v60, v60, v60 row_shr:8 row_mask:0xf bank_mask:0xf
	v_add_f32_dpp v64, v64, v64 row_shr:8 row_mask:0xf bank_mask:0xf
	v_add_f32_dpp v68, v68, v68 row_shr:8 row_mask:0xf bank_mask:0xf
	v_add_f32_dpp v72, v72, v72 row_shr:8 row_mask:0xf bank_mask:0xf
	v_add_f32_dpp v76, v76, v76 row_shr:8 row_mask:0xf bank_mask:0xf
	s_mov_b64 s[28:29], exec
	s_mov_b32 exec_lo, 0xf000f000
	s_mov_b32 exec_hi, 0xf000f000
	ds_write_b32 v47, v48
	ds_write_b32 v47, v52 offset:64
	ds_write_b32 v47, v56 offset:128
	ds_write_b32 v47, v60 offset:192
	ds_write_b32 v47, v64 offset:256
	ds_write_b32 v47, v68 offset:320
	ds_write_b32 v47, v72 offset:384
	ds_write_b32 v47, v76 offset:448
	s_mov_b64 exec, s[4:5]
	v_mov_b32_e32 v44, s37
	ds_write_b64 v44, v[42:43] offset:512
	s_mov_b64 exec, s[28:29]
	v_lshrrev_b32_e32 v42, 7, v0
	s_movk_i32 s4, 0x1080
	v_mov_b32_e32 v43, 0x23440
	s_waitcnt vmcnt(11)
	v_mad_u32_u24 v59, v42, s4, v43
	s_load_dword s6, s[22:23], 0x0
	s_waitcnt lgkmcnt(0)
	s_barrier
	ds_read_b32 v46, v59 offset:512
	ds_read_b32 v47, v59 offset:1040
	ds_read_b32 v50, v59 offset:1568
	ds_read_b32 v51, v59 offset:2096
	ds_read_b64 v[42:43], v59 offset:1040
	ds_read_b64 v[44:45], v59 offset:512
	s_mov_b32 s4, 0xff800000
	s_waitcnt vmcnt(8)
	v_cvt_pk_bf16_f32 v30, v30, v31
	v_cvt_pk_bf16_f32 v31, v32, v33
	s_waitcnt lgkmcnt(4)
	v_max3_f32 v52, v46, s4, v47
	ds_read_b64 v[46:47], v59 offset:2096
	ds_read_b64 v[48:49], v59 offset:1568
	s_waitcnt lgkmcnt(4)
	v_max3_f32 v54, v52, v50, v51
	ds_read_b32 v55, v59 offset:2624
	ds_read_b32 v56, v59 offset:3152
	ds_read_b32 v58, v59 offset:3680
	ds_read_b32 v60, v59 offset:4208
	ds_read_b64 v[50:51], v59 offset:3152
	ds_read_b64 v[52:53], v59 offset:2624
	s_waitcnt lgkmcnt(4)
	v_max3_f32 v61, v54, v55, v56
	ds_read_b64 v[54:55], v59 offset:4208
	ds_read_b64 v[56:57], v59 offset:3680
	s_waitcnt lgkmcnt(4)
	v_max3_f32 v63, v61, v58, v60
	v_and_b32_e32 v60, 0x1fc, v130
	v_sub_f32_e32 v44, v44, v63
	v_sub_f32_e32 v42, v42, v63
	v_exp_f32_e32 v58, v44
	v_add_u32_e32 v44, v59, v60
	v_exp_f32_e32 v62, v42
	v_sub_f32_e32 v42, v48, v63
	v_exp_f32_e32 v64, v42
	v_add_u32_e32 v42, 0x400, v44
	ds_read2_b32 v[66:67], v42 offset0:8 offset1:140
	v_sub_f32_e32 v42, v46, v63
	ds_read2_b32 v[60:61], v44 offset1:132
	v_exp_f32_e32 v68, v42
	s_waitcnt lgkmcnt(4)
	v_sub_f32_e32 v42, v52, v63
	v_exp_f32_e32 v70, v42
	v_add_u32_e32 v42, 0x800, v44
	ds_read2_b32 v[72:73], v42 offset0:16 offset1:148
	v_sub_f32_e32 v42, v50, v63
	s_waitcnt vmcnt(7)
	v_exp_f32_e32 v74, v42
	s_waitcnt lgkmcnt(3)
	v_sub_f32_e32 v42, v56, v63
	v_exp_f32_e32 v76, v42
	v_add_u32_e32 v42, 0xc00, v44
	s_waitcnt vmcnt(6)
	ds_read2_b32 v[78:79], v42 offset0:24 offset1:156
	v_sub_f32_e32 v42, v54, v63
	s_waitcnt lgkmcnt(2)
	v_mov_b32_e32 v44, v60
	v_exp_f32_e32 v80, v42
	v_pk_fma_f32 v[44:45], v[44:45], v[58:59], 0 op_sel_hi:[1,0,0]
	v_mov_b32_e32 v42, v61
	v_pk_fma_f32 v[42:43], v[42:43], v[62:63], v[44:45] op_sel_hi:[1,0,1]
	v_mov_b32_e32 v48, v66
	v_pk_fma_f32 v[42:43], v[48:49], v[64:65], v[42:43] op_sel_hi:[1,0,1]
	v_mov_b32_e32 v46, v67
	v_pk_fma_f32 v[42:43], v[46:47], v[68:69], v[42:43] op_sel_hi:[1,0,1]
	s_waitcnt lgkmcnt(1)
	v_mov_b32_e32 v52, v72
	v_pk_fma_f32 v[42:43], v[52:53], v[70:71], v[42:43] op_sel_hi:[1,0,1]
	v_mov_b32_e32 v50, v73
	v_pk_fma_f32 v[42:43], v[50:51], v[74:75], v[42:43] op_sel_hi:[1,0,1]
	s_waitcnt lgkmcnt(0)
	v_mov_b32_e32 v56, v78
	v_pk_fma_f32 v[42:43], v[56:57], v[76:77], v[42:43] op_sel_hi:[1,0,1]
	v_mov_b32_e32 v54, v79
	v_pk_fma_f32 v[42:43], v[54:55], v[80:81], v[42:43] op_sel_hi:[1,0,1]
	v_cvt_pk_bf16_f32 v32, v26, v27
	v_div_scale_f32 v44, s[4:5], v43, v43, v42
	v_rcp_f32_e32 v45, v44
	s_movk_i32 s4, 0x600
	v_cvt_pk_bf16_f32 v33, v28, v29
	v_cvt_pk_bf16_f32 v22, v22, v23
	v_fma_f32 v46, -v44, v45, 1.0
	v_fmac_f32_e32 v45, v46, v45
	v_div_scale_f32 v46, vcc, v42, v43, v42
	v_mul_f32_e32 v47, v46, v45
	v_fma_f32 v48, -v44, v47, v46
	v_fmac_f32_e32 v47, v48, v45
	v_fma_f32 v44, -v44, v47, v46
	v_div_fmas_f32 v44, v44, v45, v47
	v_div_fixup_f32 v42, v44, v43, v42
	v_fma_f32 v42, v42, -2.0, 1.0
	v_add_u32_e32 v43, 0x22400, v130
	ds_write_b32 v43, v42
	v_lshlrev_b32_e32 v42, 9, v0
	v_and_or_b32 v42, v42, s4, v132
	v_add_u32_e32 v50, 0x22400, v42
	s_waitcnt lgkmcnt(0)
	s_barrier
	ds_read_b128 v[42:45], v50
	ds_read_b128 v[46:49], v50 offset:16
	v_cvt_pk_bf16_f32 v23, v24, v25
	v_cvt_pk_bf16_f32 v24, v18, v19
	v_cvt_pk_bf16_f32 v25, v20, v21
	s_waitcnt lgkmcnt(1)
	v_cvt_pk_bf16_f32 v26, v42, v43
	v_cvt_pk_bf16_f32 v27, v44, v45
	s_waitcnt lgkmcnt(0)
	v_cvt_pk_bf16_f32 v28, v46, v47
	v_cvt_pk_bf16_f32 v29, v48, v49
	ds_read_b128 v[42:45], v50 offset:144
	s_waitcnt vmcnt(4)
	v_cvt_pk_bf16_f32 v14, v14, v15
	v_mfma_f32_16x16x32_bf16 v[26:29], v[30:33], v[26:29], 0
	ds_read_b128 v[30:33], v50 offset:128
	v_cvt_pk_bf16_f32 v15, v16, v17
	s_waitcnt lgkmcnt(1)
	v_cvt_pk_bf16_f32 v20, v42, v43
	v_cvt_pk_bf16_f32 v21, v44, v45
	v_cvt_pk_bf16_f32 v16, v10, v11
	s_waitcnt lgkmcnt(0)
	v_cvt_pk_bf16_f32 v18, v30, v31
	v_cvt_pk_bf16_f32 v19, v32, v33
	v_cvt_pk_bf16_f32 v17, v12, v13
	s_waitcnt vmcnt(2)
	v_cvt_pk_bf16_f32 v6, v6, v7
	v_mfma_f32_16x16x32_bf16 v[18:21], v[22:25], v[18:21], v[26:29]
	ds_read_b128 v[22:25], v50 offset:256
	v_cvt_pk_bf16_f32 v7, v8, v9
	v_cvt_pk_bf16_f32 v8, v2, v3
	ds_read_b128 v[26:29], v50 offset:272
	v_cvt_pk_bf16_f32 v9, v4, v5
	s_waitcnt lgkmcnt(1)
	v_cvt_pk_bf16_f32 v10, v22, v23
	v_cvt_pk_bf16_f32 v11, v24, v25
	s_mov_b32 s4, 0x3f200000
	s_waitcnt lgkmcnt(0)
	v_cvt_pk_bf16_f32 v12, v26, v27
	v_cvt_pk_bf16_f32 v13, v28, v29
	s_nop 1
	v_mfma_f32_16x16x32_bf16 v[10:13], v[14:17], v[10:13], v[18:21]
	ds_read_b128 v[14:17], v50 offset:384
	s_nop 1
	ds_read_b128 v[18:21], v50 offset:400
	s_waitcnt lgkmcnt(1)
	v_cvt_pk_bf16_f32 v2, v14, v15
	v_cvt_pk_bf16_f32 v3, v16, v17
	s_waitcnt lgkmcnt(0)
	v_cvt_pk_bf16_f32 v4, v18, v19
	v_cvt_pk_bf16_f32 v5, v20, v21
	s_nop 1
	v_mfma_f32_16x16x32_bf16 v[2:5], v[6:9], v[2:5], v[10:13]
	s_waitcnt vmcnt(1)
	s_nop 6
	v_add_f32_e32 v2, v2, v38
	v_add_f32_e32 v3, v3, v39
	v_add_f32_e32 v4, v4, v40
	v_add_f32_e32 v5, v5, v41
	v_mul_f32_e32 v6, 0x4038aa3b, v2
	v_mul_f32_e32 v7, 0x4038aa3b, v3
	v_mul_f32_e32 v8, 0x4038aa3b, v4
	v_mul_f32_e32 v9, 0x4038aa3b, v5
	v_exp_f32_e32 v6, v6
	v_exp_f32_e32 v7, v7
	v_exp_f32_e32 v8, v8
	v_exp_f32_e32 v9, v9
	v_add_f32_e32 v6, 1.0, v6
	v_add_f32_e32 v7, 1.0, v7
	v_add_f32_e32 v8, 1.0, v8
	v_add_f32_e32 v9, 1.0, v9
	v_rcp_f32_e32 v6, v6
	v_rcp_f32_e32 v7, v7
	v_rcp_f32_e32 v8, v8
	v_rcp_f32_e32 v9, v9
	v_fma_f32 v2, v6, -2.0, 1.0
	v_fma_f32 v3, v7, -2.0, 1.0
	v_fma_f32 v4, v8, -2.0, 1.0
	v_fma_f32 v5, v9, -2.0, 1.0
	v_cmp_gt_u32_e32 vcc, 4, v202
	s_and_saveexec_b64 s[4:5], vcc
	s_andn2_b32 s3, s3, 63
	v_lshl_or_b32 v6, v202, 9, v203
	v_add_u32_e32 v6, s3, v6
	v_add_u32_e32 v6, 0x22c00, v6
	ds_write_b128 v6, v[2:5]
	s_or_b64 exec, exec, s[4:5]
	s_waitcnt vmcnt(0)
	v_fma_f32 v2, v2, v34, 0
	v_fmac_f32_e32 v2, v3, v35
	v_fmac_f32_e32 v2, v4, v36
	v_fmac_f32_e32 v2, v5, v37
	ds_bpermute_b32 v3, v201, v2
	v_cmp_gt_u32_e32 vcc, 4, v131
	s_waitcnt lgkmcnt(0)
	v_add_f32_e32 v2, v2, v3
	ds_bpermute_b32 v3, v200, v2
	s_and_saveexec_b64 s[4:5], vcc
	s_cbranch_execz .LBB0_78
	v_add_u32_e32 v1, s30, v1
	v_add_u32_e32 v1, 0x23440, v1
	s_waitcnt lgkmcnt(0)
	v_add_f32_e32 v2, v2, v3
	ds_write_b32 v1, v2
